# att7_pack_P_fragments_between_first_PV_mfmas
# speedup vs baseline: 1.0108x; 1.0095x over previous
; __device__ __forceinline__ void qkt64c(f32x16& p0, f32x16& p1, const char* Ks, const bf16x8* qr, const f32x16& cinit, int r32, int hi) {
; #pragma unroll
;     for (int d0 = 0; d0 < 4; ++d0) { const int cb = (d0 * 16 + hi * 8) * 2;
;         const bf16x8 b0 = *reinterpret_cast<const bf16x8*>(Ks + kswz<64>(r32, cb));
;         const bf16x8 b1 = *reinterpret_cast<const bf16x8*>(Ks + kswz<64>(32 + r32, cb));
;         if (d0 == 0) { p0 = __builtin_amdgcn_mfma_f32_32x32x16_bf16(b0, qr[0], cinit, 0, 0, 0); p1 = __builtin_amdgcn_mfma_f32_32x32x16_bf16(b1, qr[0], cinit, 0, 0, 0); }
;         else { p0 = __builtin_amdgcn_mfma_f32_32x32x16_bf16(b0, qr[d0], p0, 0, 0, 0); p1 = __builtin_amdgcn_mfma_f32_32x32x16_bf16(b1, qr[d0], p1, 0, 0, 0); } }
; }
.LBB0_823:
	s_lshl_b32 s2, s42, 13
	s_add_i32 s2, s2, 0
	v_add_u32_e32 v128, s2, v223
	ds_read_b128 v[144:147], v128 offset:49152
	v_add_u32_e32 v129, s2, v226
	ds_read_b128 v[148:151], v129 offset:49152
	v_add_u32_e32 v130, s2, v228
	ds_read_b128 v[152:155], v130 offset:49152
	v_add_u32_e32 v131, s2, v229
	ds_read_b128 v[156:159], v131 offset:49152
	ds_read_b128 v[232:235], v128 offset:53248
	ds_read_b128 v[236:239], v129 offset:53248
	ds_read_b128 v[240:243], v130 offset:53248
	ds_read_b128 v[244:247], v131 offset:53248
	v_lshl_add_u64 v[202:203], v[200:201], 0, s[64:65]
	s_mov_b32 s2, 0x8a40000
	v_add_co_u32_e32 v64, vcc, s2, v202
	s_mov_b32 s2, 0x8a50000
	s_nop 0
	v_addc_co_u32_e32 v65, vcc, 0, v203, vcc
	v_add_co_u32_e32 v66, vcc, s2, v202
	v_lshl_add_u64 v[204:205], v[198:199], 0, s[64:65]
	s_nop 0
	v_addc_co_u32_e32 v67, vcc, 0, v203, vcc
	s_mov_b32 s2, 0x6a40000
	global_load_dwordx4 v[178:181], v[64:65], off
	global_load_dwordx4 v[182:185], v[66:67], off
	v_add_co_u32_e32 v64, vcc, s2, v204
	s_nop 1
	v_addc_co_u32_e32 v65, vcc, 0, v205, vcc
	global_load_dwordx4 v[186:189], v[64:65], off
	v_exp_f32_e32 v190, v120
	v_exp_f32_e32 v191, v121
	v_add_f32_e32 v120, v96, v97
	v_add_f32_e32 v121, v98, v99
	s_waitcnt lgkmcnt(7)
	v_mfma_f32_32x32x16_bf16 v[128:143], v[144:147], v[162:165], v[80:95]
	v_exp_f32_e32 v192, v122
	v_add_f32_e32 v120, v120, v121
	v_add_f32_e32 v121, v100, v101
	v_add_f32_e32 v122, v102, v103
	v_exp_f32_e32 v193, v123
	s_waitcnt lgkmcnt(6)
	v_mfma_f32_32x32x16_bf16 v[128:143], v[148:151], v[166:169], v[128:143]
	v_add_f32_e32 v121, v121, v122
	v_add_f32_e32 v122, v104, v105
	v_add_f32_e32 v123, v106, v107
	v_add_f32_e32 v122, v122, v123
	v_add_f32_e32 v123, v108, v109
	s_waitcnt lgkmcnt(5)
	v_mfma_f32_32x32x16_bf16 v[128:143], v[152:155], v[170:173], v[128:143]
	v_add_f32_e32 v208, v110, v111
	v_add_f32_e32 v123, v123, v208
	v_add_f32_e32 v208, v112, v113
	v_add_f32_e32 v209, v114, v115
	v_add_f32_e32 v208, v208, v209
	s_waitcnt lgkmcnt(4)
	v_mfma_f32_32x32x16_bf16 v[128:143], v[156:159], v[174:177], v[128:143]
	v_exp_f32_e32 v124, v124
	v_exp_f32_e32 v125, v125
	s_waitcnt lgkmcnt(3)
	v_mfma_f32_32x32x16_bf16 v[144:159], v[232:235], v[162:165], v[80:95]
	v_lshl_add_u32 v234, s12, 14, v217
	ds_read_b64_tr_b16 v[64:65], v234 offset:0
	ds_read_b64_tr_b16 v[66:67], v234 offset:0x800
	ds_read_b64_tr_b16 v[68:69], v234 offset:0x1000
	ds_read_b64_tr_b16 v[70:71], v234 offset:0x1800
	ds_read_b64_tr_b16 v[72:73], v234 offset:0x2000
	ds_read_b64_tr_b16 v[74:75], v234 offset:0x2800
	ds_read_b64_tr_b16 v[76:77], v234 offset:0x3000
	ds_read_b64_tr_b16 v[78:79], v234 offset:0x3800
	v_exp_f32_e32 v126, v126
	v_exp_f32_e32 v127, v127
	v_add_f32_e32 v120, v208, v120
	v_add_f32_e32 v208, v116, v117
	v_add_f32_e32 v209, v118, v119
	v_add_f32_e32 v208, v208, v209
	v_add_f32_e32 v121, v208, v121
	s_waitcnt lgkmcnt(10)
	v_mfma_f32_32x32x16_bf16 v[144:159], v[236:239], v[166:169], v[144:159]
	v_add_f32_e32 v208, v190, v191
	v_add_f32_e32 v209, v192, v193
	v_add_f32_e32 v208, v208, v209
	v_add_f32_e32 v122, v122, v208
	v_add_f32_e32 v208, v124, v125
	v_add_f32_e32 v209, v126, v127
	v_add_f32_e32 v208, v208, v209
	s_waitcnt lgkmcnt(9)
	v_mfma_f32_32x32x16_bf16 v[144:159], v[240:243], v[170:173], v[144:159]
	v_add_f32_e32 v123, v123, v208
	v_add_f32_e32 v120, v120, v121
	v_add_f32_e32 v121, v122, v123
	v_add_f32_e32 v231, v120, v121
	v_mov_b32_e32 v232, v231
	v_cvt_pk_bf16_f32 v96, v96, v97
	v_cvt_pk_bf16_f32 v97, v98, v99
	s_waitcnt lgkmcnt(8)
	v_mfma_f32_32x32x16_bf16 v[144:159], v[244:247], v[174:177], v[144:159]
	v_cvt_pk_bf16_f32 v98, v100, v101
	v_cvt_pk_bf16_f32 v99, v102, v103
	v_cvt_pk_bf16_f32 v120, v104, v105
	v_cvt_pk_bf16_f32 v121, v106, v107
	v_cvt_pk_bf16_f32 v122, v108, v109
	v_cvt_pk_bf16_f32 v123, v110, v111
	v_permlane32_swap_b32_e32 v96, v98
	v_permlane32_swap_b32_e32 v97, v99
	v_cvt_pk_bf16_f32 v104, v112, v113
	v_cvt_pk_bf16_f32 v105, v114, v115
	v_cvt_pk_bf16_f32 v106, v116, v117
	v_cvt_pk_bf16_f32 v107, v118, v119
	s_waitcnt lgkmcnt(0)
	v_mfma_f32_32x32x16_bf16 v[0:15], v[96:99], v[64:67], v[0:15]
	v_permlane32_swap_b32_e32 v120, v122
	v_permlane32_swap_b32_e32 v121, v123
	v_cvt_pk_bf16_f32 v100, v190, v191
	v_cvt_pk_bf16_f32 v101, v192, v193
	v_cvt_pk_bf16_f32 v102, v124, v125
	v_cvt_pk_bf16_f32 v103, v126, v127
	v_mfma_f32_32x32x16_bf16 v[0:15], v[120:123], v[68:71], v[0:15]
	v_permlane32_swap_b32_e32 v104, v106
	v_permlane32_swap_b32_e32 v105, v107
	ds_read_b64_tr_b16 v[236:237], v234 offset:0x200
	ds_read_b64_tr_b16 v[238:239], v234 offset:0xa00
	ds_read_b64_tr_b16 v[240:241], v234 offset:0x1200
	ds_read_b64_tr_b16 v[242:243], v234 offset:0x1a00
	ds_read_b64_tr_b16 v[244:245], v234 offset:0x2200
	ds_read_b64_tr_b16 v[246:247], v234 offset:0x2a00
	ds_read_b64_tr_b16 v[190:191], v234 offset:0x3200
	ds_read_b64_tr_b16 v[192:193], v234 offset:0x3a00
	v_mfma_f32_32x32x16_bf16 v[0:15], v[104:107], v[72:75], v[0:15]
	v_permlane32_swap_b32_e32 v100, v102
	v_permlane32_swap_b32_e32 v101, v103
	v_permlane32_swap_b32_e32 v231, v232
	v_max_f32_e32 v108, v128, v129
	v_max3_f32 v109, v130, v131, v145
	v_max3_f32 v108, v108, v144, v146
	v_max3_f32 v108, v108, v147, v132
	v_max3_f32 v109, v109, v134, v135
	v_mfma_f32_32x32x16_bf16 v[0:15], v[100:103], v[76:79], v[0:15]
	v_max3_f32 v208, v108, v133, v148
	v_max3_f32 v209, v109, v150, v151
	ds_read_b64_tr_b16 v[124:125], v234 offset:0x400
	ds_read_b64_tr_b16 v[126:127], v234 offset:0xc00
	ds_read_b64_tr_b16 v[116:117], v234 offset:0x1400
	ds_read_b64_tr_b16 v[118:119], v234 offset:0x1c00
	ds_read_b64_tr_b16 v[112:113], v234 offset:0x2400
	ds_read_b64_tr_b16 v[114:115], v234 offset:0x2c00
	ds_read_b64_tr_b16 v[108:109], v234 offset:0x3400
	ds_read_b64_tr_b16 v[110:111], v234 offset:0x3c00
	s_waitcnt lgkmcnt(8)
	v_mfma_f32_32x32x16_bf16 v[48:63], v[96:99], v[236:239], v[48:63]
	v_max3_f32 v208, v208, v149, v136
	v_max3_f32 v209, v209, v138, v139
	v_max3_f32 v208, v208, v137, v152
	v_max3_f32 v209, v209, v154, v155
	v_max3_f32 v208, v208, v153, v140
	v_max3_f32 v209, v209, v142, v143
	v_max3_f32 v208, v208, v141, v156
	v_mfma_f32_32x32x16_bf16 v[48:63], v[120:123], v[240:243], v[48:63]
	v_max3_f32 v209, v209, v158, v159
	v_max3_f32 v208, v208, v157, v209
	v_mov_b32_e32 v209, v208
	s_nop 1
	v_permlane32_swap_b32_e32 v208, v209
	v_mfma_f32_32x32x16_bf16 v[48:63], v[104:107], v[244:247], v[48:63]
	v_max_f32_e32 v233, v208, v209
	v_mfma_f32_32x32x16_bf16 v[48:63], v[100:103], v[190:193], v[48:63]
	s_mov_b32 s2, 0x4138aa3b
	v_cmp_ge_f32_e32 vcc, s2, v233
	s_cmp_eq_u64 vcc, exec
	s_cbranch_scc0 .LBB0_836
	v_mov_b32_e32 v233, 1.0

; #define SBAR() __builtin_amdgcn_sched_barrier(0)
; #define SLOAD(k0) do { vs0 = *reinterpret_cast<const bf16x8*>(&Vh[(size_t)((k0) + sr) * DM + sc]); vs1 = *reinterpret_cast<const bf16x8*>(&Vh[(size_t)((k0) + 32 + sr) * DM + sc]); \
;     ks = *reinterpret_cast<const bf16x8*>(&Kh[(size_t)((k0) + kr) * DM + kc]); } while (0)
; #define SWRITE(s) do { *(bf16x8*)(V_lds + (s) * SHM_V + vst0) = vs0; *(bf16x8*)(V_lds + (s) * SHM_V + vst1) = vs1; *(bf16x8*)(K_lds + (s) * SHM_K64 + kst) = ks; } while (0)
; #define RESC(a) do { if (__any((a) < 1.f)) { if (hi == 0) al_l[r32] = (a); asm volatile("s_waitcnt lgkmcnt(0)" ::: "memory"); \
;     _Pragma("unroll") for (int d = 0; d < 4; ++d) _Pragma("unroll") for (int r = 0; r < 16; ++r) o[d][r] *= al_l[crow(r, hi)]; } } while (0)
; #define ROT() do { s_prev = s_cur; s_cur = s_next; s_next = (s_next == DA_NBUF - 1) ? 0 : s_next + 1; } while (0)
; __device__ __forceinline__ void diff_pass(const bf16_t* __restrict__ Qb, const bf16_t* __restrict__ Kh, const bf16_t* __restrict__ Vh, int seq, char* lds, f32x16 (&o)[4], const int wave_) {
;     ...
;         SBAR(); qkt64c(pB0, pB1, K_lds + s_cur * SHM_K64, qr, negm, r32, hi); FIN(pA0, pA1, alA); SBAR();
;         YSEG(pB0, pB1, alB, s_prev);
;         SWRITE(s_next); RESC(alB); __syncthreads(); ROT();
;         SLOAD((j + 2) * 64);
;         SBAR(); qkt64c(pA0, pA1, K_lds + s_cur * SHM_K64, qr, negm, r32, hi); FIN(pB0, pB1, alB); SBAR();
;         YSEG(pA0, pA1, alA, s_prev);
.LBB0_829:
	v_add_co_u32_e32 v96, vcc, 0x8a60000, v202
	s_waitcnt lgkmcnt(0)
	s_nop 0
	v_addc_co_u32_e32 v97, vcc, 0, v203, vcc
	v_add_co_u32_e32 v98, vcc, 0x8a70000, v202
	s_nop 1
	v_addc_co_u32_e32 v99, vcc, 0, v203, vcc
	v_add_co_u32_e32 v100, vcc, 0x6a60000, v204
	s_nop 1
	v_addc_co_u32_e32 v101, vcc, 0, v205, vcc
	s_barrier
	v_add_u32_e32 v102, s2, v223
	ds_read_b128 v[112:115], v102 offset:49152
	v_add_u32_e32 v103, s2, v226
	ds_read_b128 v[116:119], v103 offset:49152
	v_add_u32_e32 v104, s2, v228
	ds_read_b128 v[120:123], v104 offset:49152
	v_add_u32_e32 v105, s2, v229
	ds_read_b128 v[124:127], v105 offset:49152
	ds_read_b128 v[190:193], v102 offset:53248
	ds_read_b128 v[202:205], v103 offset:53248
	ds_read_b128 v[234:237], v104 offset:53248
	ds_read_b128 v[238:241], v105 offset:53248
	global_load_dwordx4 v[178:181], v[96:97], off
	global_load_dwordx4 v[182:185], v[98:99], off
	global_load_dwordx4 v[186:189], v[100:101], off
	v_exp_f32_e32 v208, v152
	v_exp_f32_e32 v209, v153
	v_add_f32_e32 v152, v128, v129
	v_add_f32_e32 v153, v130, v131
	s_waitcnt lgkmcnt(7)
	v_mfma_f32_32x32x16_bf16 v[96:111], v[112:115], v[162:165], v[80:95]
	v_exp_f32_e32 v210, v154
	v_add_f32_e32 v152, v152, v153
	v_add_f32_e32 v153, v132, v133
	v_add_f32_e32 v154, v134, v135
	v_exp_f32_e32 v211, v155
	s_waitcnt lgkmcnt(6)
	v_mfma_f32_32x32x16_bf16 v[96:111], v[116:119], v[166:169], v[96:111]
	v_add_f32_e32 v153, v153, v154
	v_add_f32_e32 v154, v136, v137
	v_add_f32_e32 v155, v138, v139
	v_add_f32_e32 v154, v154, v155
	v_add_f32_e32 v155, v140, v141
	s_waitcnt lgkmcnt(5)
	v_mfma_f32_32x32x16_bf16 v[96:111], v[120:123], v[170:173], v[96:111]
	v_exp_f32_e32 v156, v156
	v_exp_f32_e32 v157, v157
	v_exp_f32_e32 v158, v158
	v_exp_f32_e32 v159, v159
	s_waitcnt lgkmcnt(4)
	v_mfma_f32_32x32x16_bf16 v[96:111], v[124:127], v[174:177], v[96:111]
	s_waitcnt lgkmcnt(3)
	v_mfma_f32_32x32x16_bf16 v[112:127], v[190:193], v[162:165], v[80:95]
	v_add_f32_e32 v190, v142, v143
	v_add_f32_e32 v155, v155, v190
	v_add_f32_e32 v190, v144, v145
	v_add_f32_e32 v191, v146, v147
	v_add_f32_e32 v190, v190, v191
	v_add_f32_e32 v152, v152, v190
	v_add_f32_e32 v190, v148, v149
	s_waitcnt lgkmcnt(2)
	v_mfma_f32_32x32x16_bf16 v[112:127], v[202:205], v[166:169], v[112:127]
	v_lshl_add_u32 v205, s42, 14, v217
	ds_read_b64_tr_b16 v[64:65], v205 offset:0
	ds_read_b64_tr_b16 v[66:67], v205 offset:0x800
	ds_read_b64_tr_b16 v[68:69], v205 offset:0x1000
	ds_read_b64_tr_b16 v[70:71], v205 offset:0x1800
	ds_read_b64_tr_b16 v[72:73], v205 offset:0x2000
	ds_read_b64_tr_b16 v[74:75], v205 offset:0x2800
	ds_read_b64_tr_b16 v[76:77], v205 offset:0x3000
	ds_read_b64_tr_b16 v[78:79], v205 offset:0x3800
	v_add_f32_e32 v191, v150, v151
	v_add_f32_e32 v190, v190, v191
	v_add_f32_e32 v153, v153, v190
	v_add_f32_e32 v190, v208, v209
	v_add_f32_e32 v191, v210, v211
	v_add_f32_e32 v190, v190, v191
	v_add_f32_e32 v154, v154, v190
	s_waitcnt lgkmcnt(9)
	v_mfma_f32_32x32x16_bf16 v[112:127], v[234:237], v[170:173], v[112:127]
	v_add_f32_e32 v190, v156, v157
	v_add_f32_e32 v191, v158, v159
	v_add_f32_e32 v190, v190, v191
	v_add_f32_e32 v155, v155, v190
	v_add_f32_e32 v152, v152, v153
	v_add_f32_e32 v153, v154, v155
	v_add_f32_e32 v203, v152, v153
	s_waitcnt lgkmcnt(8)
	v_mfma_f32_32x32x16_bf16 v[112:127], v[238:241], v[174:177], v[112:127]
	v_mov_b32_e32 v204, v203
	v_cvt_pk_bf16_f32 v152, v128, v129
	v_cvt_pk_bf16_f32 v153, v130, v131
	v_cvt_pk_bf16_f32 v154, v132, v133
	v_cvt_pk_bf16_f32 v155, v134, v135
	v_cvt_pk_bf16_f32 v136, v136, v137
	v_cvt_pk_bf16_f32 v137, v138, v139
	v_cvt_pk_bf16_f32 v138, v140, v141
	v_cvt_pk_bf16_f32 v139, v142, v143
	v_permlane32_swap_b32_e32 v152, v154
	v_permlane32_swap_b32_e32 v153, v155
	v_cvt_pk_bf16_f32 v132, v144, v145
	v_cvt_pk_bf16_f32 v133, v146, v147
	v_cvt_pk_bf16_f32 v134, v148, v149
	v_cvt_pk_bf16_f32 v135, v150, v151
	s_waitcnt lgkmcnt(0)
	v_mfma_f32_32x32x16_bf16 v[0:15], v[152:155], v[64:67], v[0:15]
	v_permlane32_swap_b32_e32 v136, v138
	v_permlane32_swap_b32_e32 v137, v139
	v_cvt_pk_bf16_f32 v128, v208, v209
	v_cvt_pk_bf16_f32 v129, v210, v211
	v_cvt_pk_bf16_f32 v130, v156, v157
	v_cvt_pk_bf16_f32 v131, v158, v159
	v_mfma_f32_32x32x16_bf16 v[0:15], v[136:139], v[68:71], v[0:15]
	v_permlane32_swap_b32_e32 v132, v134
	v_permlane32_swap_b32_e32 v133, v135
	ds_read_b64_tr_b16 v[190:191], v205 offset:0x200
	ds_read_b64_tr_b16 v[192:193], v205 offset:0xa00
	ds_read_b64_tr_b16 v[234:235], v205 offset:0x1200
	ds_read_b64_tr_b16 v[236:237], v205 offset:0x1a00
	ds_read_b64_tr_b16 v[238:239], v205 offset:0x2200
	ds_read_b64_tr_b16 v[240:241], v205 offset:0x2a00
	ds_read_b64_tr_b16 v[242:243], v205 offset:0x3200
	ds_read_b64_tr_b16 v[244:245], v205 offset:0x3a00
	v_mfma_f32_32x32x16_bf16 v[0:15], v[132:135], v[72:75], v[0:15]
	v_permlane32_swap_b32_e32 v128, v130
	v_permlane32_swap_b32_e32 v129, v131
	v_permlane32_swap_b32_e32 v203, v204
	v_max_f32_e32 v140, v96, v97
	v_max3_f32 v140, v140, v112, v114
	v_max3_f32 v141, v98, v99, v113
	v_max3_f32 v140, v140, v115, v100
	v_max3_f32 v141, v141, v102, v103
	v_mfma_f32_32x32x16_bf16 v[0:15], v[128:131], v[76:79], v[0:15]
	v_max3_f32 v202, v140, v101, v116
	v_max3_f32 v208, v141, v118, v119
	ds_read_b64_tr_b16 v[156:157], v205 offset:0x400
	ds_read_b64_tr_b16 v[158:159], v205 offset:0xc00
	ds_read_b64_tr_b16 v[148:149], v205 offset:0x1400
	ds_read_b64_tr_b16 v[150:151], v205 offset:0x1c00
	ds_read_b64_tr_b16 v[144:145], v205 offset:0x2400
	ds_read_b64_tr_b16 v[146:147], v205 offset:0x2c00
	ds_read_b64_tr_b16 v[140:141], v205 offset:0x3400
	ds_read_b64_tr_b16 v[142:143], v205 offset:0x3c00
	s_waitcnt lgkmcnt(8)
	v_mfma_f32_32x32x16_bf16 v[48:63], v[152:155], v[190:193], v[48:63]
	v_max3_f32 v190, v202, v117, v104
	v_max3_f32 v191, v208, v106, v107
	v_max3_f32 v190, v190, v105, v120
	v_max3_f32 v191, v191, v122, v123
	v_max3_f32 v190, v190, v121, v108
	v_max3_f32 v191, v191, v110, v111
	v_max3_f32 v190, v190, v109, v124
	v_mfma_f32_32x32x16_bf16 v[48:63], v[136:139], v[234:237], v[48:63]
	v_max3_f32 v191, v191, v126, v127
	v_max3_f32 v190, v190, v125, v191
	v_mov_b32_e32 v191, v190
	s_nop 1
	v_permlane32_swap_b32_e32 v190, v191
	v_mfma_f32_32x32x16_bf16 v[48:63], v[132:135], v[238:241], v[48:63]
	v_max_f32_e32 v234, v190, v191
	v_mfma_f32_32x32x16_bf16 v[48:63], v[128:131], v[242:245], v[48:63]
	s_mov_b32 s2, 0x4138aa3b
	v_cmp_ge_f32_e32 vcc, s2, v234
	s_cmp_eq_u64 vcc, exec
	v_mov_b32_e32 v202, 1.0
	s_cbranch_scc0 .LBB0_837

; __device__ __forceinline__ void qkt64c(f32x16& p0, f32x16& p1, const char* Ks, const bf16x8* qr, const f32x16& cinit, int r32, int hi) {
; #pragma unroll
;     for (int d0 = 0; d0 < 4; ++d0) { const int cb = (d0 * 16 + hi * 8) * 2;
;         const bf16x8 b0 = *reinterpret_cast<const bf16x8*>(Ks + kswz<64>(r32, cb));
;         const bf16x8 b1 = *reinterpret_cast<const bf16x8*>(Ks + kswz<64>(32 + r32, cb));
;         if (d0 == 0) { p0 = __builtin_amdgcn_mfma_f32_32x32x16_bf16(b0, qr[0], cinit, 0, 0, 0); p1 = __builtin_amdgcn_mfma_f32_32x32x16_bf16(b1, qr[0], cinit, 0, 0, 0); }
;         else { p0 = __builtin_amdgcn_mfma_f32_32x32x16_bf16(b0, qr[d0], p0, 0, 0, 0); p1 = __builtin_amdgcn_mfma_f32_32x32x16_bf16(b1, qr[d0], p1, 0, 0, 0); } }
; }
.LBB0_846:
	s_lshl_b32 s2, s30, 13
	s_add_i32 s2, s2, 0
	v_add_u32_e32 v128, s2, v227
	ds_read_b128 v[144:147], v128 offset:49152
	v_add_u32_e32 v129, s2, v231
	ds_read_b128 v[148:151], v129 offset:49152
	v_add_u32_e32 v130, s2, v232
	ds_read_b128 v[152:155], v130 offset:49152
	v_add_u32_e32 v131, s2, v233
	ds_read_b128 v[156:159], v131 offset:49152
	ds_read_b128 v[190:193], v128 offset:53248
	ds_read_b128 v[236:239], v129 offset:53248
	ds_read_b128 v[240:243], v130 offset:53248
	ds_read_b128 v[244:247], v131 offset:53248
	v_lshl_add_u64 v[202:203], v[200:201], 0, s[64:65]
	s_mov_b32 s2, 0x8a40000
	v_add_co_u32_e32 v64, vcc, s2, v202
	s_mov_b32 s2, 0x8a50000
	s_nop 0
	v_addc_co_u32_e32 v65, vcc, 0, v203, vcc
	v_add_co_u32_e32 v66, vcc, s2, v202
	v_lshl_add_u64 v[204:205], v[198:199], 0, s[64:65]
	s_nop 0
	v_addc_co_u32_e32 v67, vcc, 0, v203, vcc
	s_mov_b32 s2, 0x6a40000
	global_load_dwordx4 v[178:181], v[64:65], off
	global_load_dwordx4 v[182:185], v[66:67], off
	v_add_co_u32_e32 v64, vcc, s2, v204
	s_nop 1
	v_addc_co_u32_e32 v65, vcc, 0, v205, vcc
	global_load_dwordx4 v[186:189], v[64:65], off offset:128
	v_exp_f32_e32 v208, v120
	v_exp_f32_e32 v209, v121
	v_add_f32_e32 v120, v96, v97
	v_add_f32_e32 v121, v98, v99
	s_waitcnt lgkmcnt(7)
	v_mfma_f32_32x32x16_bf16 v[128:143], v[144:147], v[162:165], v[80:95]
	v_exp_f32_e32 v210, v122
	v_add_f32_e32 v120, v120, v121
	v_add_f32_e32 v121, v100, v101
	v_add_f32_e32 v122, v102, v103
	v_exp_f32_e32 v211, v123
	s_waitcnt lgkmcnt(6)
	v_mfma_f32_32x32x16_bf16 v[128:143], v[148:151], v[166:169], v[128:143]
	v_add_f32_e32 v121, v121, v122
	v_add_f32_e32 v122, v104, v105
	v_add_f32_e32 v123, v106, v107
	v_add_f32_e32 v122, v122, v123
	v_add_f32_e32 v123, v108, v109
	s_waitcnt lgkmcnt(5)
	v_mfma_f32_32x32x16_bf16 v[128:143], v[152:155], v[170:173], v[128:143]
	v_exp_f32_e32 v124, v124
	v_exp_f32_e32 v125, v125
	v_exp_f32_e32 v126, v126
	v_exp_f32_e32 v127, v127
	v_cvt_pk_bf16_f32 v96, v96, v97
	s_waitcnt lgkmcnt(4)
	v_mfma_f32_32x32x16_bf16 v[128:143], v[156:159], v[174:177], v[128:143]
	v_cvt_pk_bf16_f32 v97, v98, v99
	v_cvt_pk_bf16_f32 v98, v100, v101
	v_cvt_pk_bf16_f32 v99, v102, v103
	s_nop 0
	v_permlane32_swap_b32_e32 v96, v98
	s_waitcnt lgkmcnt(3)
	v_mfma_f32_32x32x16_bf16 v[144:159], v[190:193], v[162:165], v[80:95]
	v_add_f32_e32 v190, v110, v111
	v_add_f32_e32 v123, v123, v190
	v_add_f32_e32 v190, v112, v113
	v_add_f32_e32 v191, v114, v115
	v_add_f32_e32 v190, v190, v191
	v_add_f32_e32 v120, v190, v120
	v_add_f32_e32 v190, v116, v117
	s_waitcnt lgkmcnt(2)
	v_mfma_f32_32x32x16_bf16 v[144:159], v[236:239], v[166:169], v[144:159]
	v_lshl_add_u32 v238, s12, 14, v221
	ds_read_b64_tr_b16 v[64:65], v238 offset:0
	ds_read_b64_tr_b16 v[66:67], v238 offset:0x800
	ds_read_b64_tr_b16 v[68:69], v238 offset:0x1000
	ds_read_b64_tr_b16 v[70:71], v238 offset:0x1800
	ds_read_b64_tr_b16 v[72:73], v238 offset:0x2000
	ds_read_b64_tr_b16 v[74:75], v238 offset:0x2800
	ds_read_b64_tr_b16 v[76:77], v238 offset:0x3000
	ds_read_b64_tr_b16 v[78:79], v238 offset:0x3800
	v_add_f32_e32 v191, v118, v119
	v_add_f32_e32 v190, v190, v191
	v_add_f32_e32 v121, v190, v121
	v_add_f32_e32 v190, v208, v209
	v_add_f32_e32 v191, v210, v211
	v_add_f32_e32 v190, v190, v191
	v_add_f32_e32 v122, v122, v190
	s_waitcnt lgkmcnt(9)
	v_mfma_f32_32x32x16_bf16 v[144:159], v[240:243], v[170:173], v[144:159]
	v_add_f32_e32 v190, v124, v125
	v_add_f32_e32 v191, v126, v127
	v_add_f32_e32 v190, v190, v191
	v_add_f32_e32 v123, v123, v190
	v_add_f32_e32 v120, v120, v121
	v_add_f32_e32 v121, v122, v123
	v_add_f32_e32 v235, v120, v121
	s_waitcnt lgkmcnt(8)
	v_mfma_f32_32x32x16_bf16 v[144:159], v[244:247], v[174:177], v[144:159]
	v_mov_b32_e32 v236, v235
	v_cvt_pk_bf16_f32 v120, v104, v105
	v_cvt_pk_bf16_f32 v121, v106, v107
	v_cvt_pk_bf16_f32 v122, v108, v109
	v_cvt_pk_bf16_f32 v123, v110, v111
	v_permlane32_swap_b32_e32 v97, v99
	v_cvt_pk_bf16_f32 v104, v112, v113
	v_cvt_pk_bf16_f32 v105, v114, v115
	v_cvt_pk_bf16_f32 v106, v116, v117
	v_cvt_pk_bf16_f32 v107, v118, v119
	s_waitcnt lgkmcnt(0)
	v_mfma_f32_32x32x16_bf16 v[0:15], v[96:99], v[64:67], v[0:15]
	v_permlane32_swap_b32_e32 v120, v122
	v_permlane32_swap_b32_e32 v121, v123
	v_cvt_pk_bf16_f32 v100, v208, v209
	v_cvt_pk_bf16_f32 v101, v210, v211
	v_cvt_pk_bf16_f32 v102, v124, v125
	v_cvt_pk_bf16_f32 v103, v126, v127
	v_mfma_f32_32x32x16_bf16 v[0:15], v[120:123], v[68:71], v[0:15]
	v_permlane32_swap_b32_e32 v104, v106
	v_permlane32_swap_b32_e32 v105, v107
	ds_read_b64_tr_b16 v[190:191], v238 offset:0x200
	ds_read_b64_tr_b16 v[192:193], v238 offset:0xa00
	ds_read_b64_tr_b16 v[240:241], v238 offset:0x1200
	ds_read_b64_tr_b16 v[242:243], v238 offset:0x1a00
	ds_read_b64_tr_b16 v[244:245], v238 offset:0x2200
	ds_read_b64_tr_b16 v[246:247], v238 offset:0x2a00
	ds_read_b64_tr_b16 v[208:209], v238 offset:0x3200
	ds_read_b64_tr_b16 v[210:211], v238 offset:0x3a00
	v_mfma_f32_32x32x16_bf16 v[0:15], v[104:107], v[72:75], v[0:15]
	v_permlane32_swap_b32_e32 v100, v102
	v_permlane32_swap_b32_e32 v101, v103
	v_permlane32_swap_b32_e32 v235, v236
	v_max_f32_e32 v108, v128, v129
	v_max3_f32 v108, v108, v144, v146
	v_max3_f32 v109, v130, v131, v145
	v_max3_f32 v108, v108, v147, v132
	v_max3_f32 v109, v109, v134, v135
	v_mfma_f32_32x32x16_bf16 v[0:15], v[100:103], v[76:79], v[0:15]
	v_max3_f32 v237, v108, v133, v148
	v_max3_f32 v239, v109, v150, v151
	ds_read_b64_tr_b16 v[124:125], v238 offset:0x400
	ds_read_b64_tr_b16 v[126:127], v238 offset:0xc00
	ds_read_b64_tr_b16 v[116:117], v238 offset:0x1400
	ds_read_b64_tr_b16 v[118:119], v238 offset:0x1c00
	ds_read_b64_tr_b16 v[112:113], v238 offset:0x2400
	ds_read_b64_tr_b16 v[114:115], v238 offset:0x2c00
	ds_read_b64_tr_b16 v[108:109], v238 offset:0x3400
	ds_read_b64_tr_b16 v[110:111], v238 offset:0x3c00
	s_waitcnt lgkmcnt(8)
	v_mfma_f32_32x32x16_bf16 v[48:63], v[96:99], v[190:193], v[48:63]
	v_max3_f32 v190, v237, v149, v136
	v_max3_f32 v191, v239, v138, v139
	v_max3_f32 v190, v190, v137, v152
	v_max3_f32 v191, v191, v154, v155
	v_max3_f32 v190, v190, v153, v140
	v_max3_f32 v191, v191, v142, v143
	v_max3_f32 v190, v190, v141, v156
	v_mfma_f32_32x32x16_bf16 v[48:63], v[120:123], v[240:243], v[48:63]
	v_max3_f32 v191, v191, v158, v159
	v_max3_f32 v190, v190, v157, v191
	v_mov_b32_e32 v191, v190
	s_nop 1
	v_permlane32_swap_b32_e32 v190, v191
	v_mfma_f32_32x32x16_bf16 v[48:63], v[104:107], v[244:247], v[48:63]
	v_max_f32_e32 v237, v190, v191
	v_mfma_f32_32x32x16_bf16 v[48:63], v[100:103], v[208:211], v[48:63]
	s_mov_b32 s2, 0x4138aa3b
	v_cmp_ge_f32_e32 vcc, s2, v237
	s_cmp_eq_u64 vcc, exec
	s_cbranch_scc0 .LBB0_859
	v_mov_b32_e32 v237, 1.0

; #define SBAR() __builtin_amdgcn_sched_barrier(0)
; #define SLOAD(k0) do { vs0 = *reinterpret_cast<const bf16x8*>(&Vh[(size_t)((k0) + sr) * DM + sc]); vs1 = *reinterpret_cast<const bf16x8*>(&Vh[(size_t)((k0) + 32 + sr) * DM + sc]); \
;     ks = *reinterpret_cast<const bf16x8*>(&Kh[(size_t)((k0) + kr) * DM + kc]); } while (0)
; #define SWRITE(s) do { *(bf16x8*)(V_lds + (s) * SHM_V + vst0) = vs0; *(bf16x8*)(V_lds + (s) * SHM_V + vst1) = vs1; *(bf16x8*)(K_lds + (s) * SHM_K64 + kst) = ks; } while (0)
; #define RESC(a) do { if (__any((a) < 1.f)) { if (hi == 0) al_l[r32] = (a); asm volatile("s_waitcnt lgkmcnt(0)" ::: "memory"); \
;     _Pragma("unroll") for (int d = 0; d < 4; ++d) _Pragma("unroll") for (int r = 0; r < 16; ++r) o[d][r] *= al_l[crow(r, hi)]; } } while (0)
; #define ROT() do { s_prev = s_cur; s_cur = s_next; s_next = (s_next == DA_NBUF - 1) ? 0 : s_next + 1; } while (0)
; __device__ __forceinline__ void diff_pass(const bf16_t* __restrict__ Qb, const bf16_t* __restrict__ Kh, const bf16_t* __restrict__ Vh, int seq, char* lds, f32x16 (&o)[4], const int wave_) {
;     ...
;         SBAR(); qkt64c(pB0, pB1, K_lds + s_cur * SHM_K64, qr, negm, r32, hi); FIN(pA0, pA1, alA); SBAR();
;         YSEG(pB0, pB1, alB, s_prev);
;         SWRITE(s_next); RESC(alB); __syncthreads(); ROT();
;         SLOAD((j + 2) * 64);
;         SBAR(); qkt64c(pA0, pA1, K_lds + s_cur * SHM_K64, qr, negm, r32, hi); FIN(pB0, pB1, alB); SBAR();
;         YSEG(pA0, pA1, alA, s_prev);
.LBB0_852:
	v_add_co_u32_e32 v96, vcc, 0x8a60000, v202
	s_waitcnt lgkmcnt(0)
	s_nop 0
	v_addc_co_u32_e32 v97, vcc, 0, v203, vcc
	v_add_co_u32_e32 v98, vcc, 0x8a70000, v202
	s_nop 1
	v_addc_co_u32_e32 v99, vcc, 0, v203, vcc
	v_add_co_u32_e32 v100, vcc, 0x6a60000, v204
	s_nop 1
	v_addc_co_u32_e32 v101, vcc, 0, v205, vcc
	s_barrier
	v_add_u32_e32 v102, s2, v227
	ds_read_b128 v[112:115], v102 offset:49152
	v_add_u32_e32 v103, s2, v231
	ds_read_b128 v[116:119], v103 offset:49152
	v_add_u32_e32 v104, s2, v232
	ds_read_b128 v[120:123], v104 offset:49152
	v_add_u32_e32 v105, s2, v233
	ds_read_b128 v[124:127], v105 offset:49152
	ds_read_b128 v[190:193], v102 offset:53248
	ds_read_b128 v[202:205], v103 offset:53248
	ds_read_b128 v[208:211], v104 offset:53248
	ds_read_b128 v[238:241], v105 offset:53248
	global_load_dwordx4 v[178:181], v[96:97], off
	global_load_dwordx4 v[182:185], v[98:99], off
	global_load_dwordx4 v[186:189], v[100:101], off offset:128
	v_exp_f32_e32 v242, v152
	v_exp_f32_e32 v243, v153
	v_add_f32_e32 v152, v128, v129
	v_add_f32_e32 v153, v130, v131
	s_waitcnt lgkmcnt(7)
	v_mfma_f32_32x32x16_bf16 v[96:111], v[112:115], v[162:165], v[80:95]
	v_exp_f32_e32 v244, v154
	v_add_f32_e32 v152, v152, v153
	v_add_f32_e32 v153, v132, v133
	v_add_f32_e32 v154, v134, v135
	v_exp_f32_e32 v245, v155
	s_waitcnt lgkmcnt(6)
	v_mfma_f32_32x32x16_bf16 v[96:111], v[116:119], v[166:169], v[96:111]
	v_add_f32_e32 v153, v153, v154
	v_add_f32_e32 v154, v136, v137
	v_add_f32_e32 v155, v138, v139
	v_add_f32_e32 v154, v154, v155
	v_add_f32_e32 v155, v140, v141
	s_waitcnt lgkmcnt(5)
	v_mfma_f32_32x32x16_bf16 v[96:111], v[120:123], v[170:173], v[96:111]
	v_exp_f32_e32 v156, v156
	v_exp_f32_e32 v157, v157
	v_exp_f32_e32 v158, v158
	v_exp_f32_e32 v159, v159
	s_waitcnt lgkmcnt(4)
	v_mfma_f32_32x32x16_bf16 v[96:111], v[124:127], v[174:177], v[96:111]
	s_waitcnt lgkmcnt(3)
	v_mfma_f32_32x32x16_bf16 v[112:127], v[190:193], v[162:165], v[80:95]
	v_add_f32_e32 v190, v142, v143
	v_add_f32_e32 v155, v155, v190
	v_add_f32_e32 v190, v144, v145
	v_add_f32_e32 v191, v146, v147
	v_add_f32_e32 v190, v190, v191
	v_add_f32_e32 v152, v152, v190
	v_add_f32_e32 v190, v148, v149
	s_waitcnt lgkmcnt(2)
	v_mfma_f32_32x32x16_bf16 v[112:127], v[202:205], v[166:169], v[112:127]
	v_lshl_add_u32 v205, s30, 14, v221
	ds_read_b64_tr_b16 v[64:65], v205 offset:0
	ds_read_b64_tr_b16 v[66:67], v205 offset:0x800
	ds_read_b64_tr_b16 v[68:69], v205 offset:0x1000
	ds_read_b64_tr_b16 v[70:71], v205 offset:0x1800
	ds_read_b64_tr_b16 v[72:73], v205 offset:0x2000
	ds_read_b64_tr_b16 v[74:75], v205 offset:0x2800
	ds_read_b64_tr_b16 v[76:77], v205 offset:0x3000
	ds_read_b64_tr_b16 v[78:79], v205 offset:0x3800
	v_add_f32_e32 v191, v150, v151
	v_add_f32_e32 v190, v190, v191
	v_add_f32_e32 v153, v153, v190
	v_add_f32_e32 v190, v242, v243
	v_add_f32_e32 v191, v244, v245
	v_add_f32_e32 v190, v190, v191
	v_add_f32_e32 v154, v154, v190
	s_waitcnt lgkmcnt(9)
	v_mfma_f32_32x32x16_bf16 v[112:127], v[208:211], v[170:173], v[112:127]
	v_add_f32_e32 v190, v156, v157
	v_add_f32_e32 v191, v158, v159
	v_add_f32_e32 v190, v190, v191
	v_add_f32_e32 v155, v155, v190
	v_add_f32_e32 v152, v152, v153
	v_add_f32_e32 v153, v154, v155
	v_add_f32_e32 v203, v152, v153
	s_waitcnt lgkmcnt(8)
	v_mfma_f32_32x32x16_bf16 v[112:127], v[238:241], v[174:177], v[112:127]
	v_mov_b32_e32 v204, v203
	v_cvt_pk_bf16_f32 v152, v128, v129
	v_cvt_pk_bf16_f32 v153, v130, v131
	v_cvt_pk_bf16_f32 v154, v132, v133
	v_cvt_pk_bf16_f32 v155, v134, v135
	v_cvt_pk_bf16_f32 v136, v136, v137
	v_cvt_pk_bf16_f32 v137, v138, v139
	v_cvt_pk_bf16_f32 v138, v140, v141
	v_cvt_pk_bf16_f32 v139, v142, v143
	v_permlane32_swap_b32_e32 v152, v154
	v_permlane32_swap_b32_e32 v153, v155
	v_cvt_pk_bf16_f32 v132, v144, v145
	v_cvt_pk_bf16_f32 v133, v146, v147
	v_cvt_pk_bf16_f32 v134, v148, v149
	v_cvt_pk_bf16_f32 v135, v150, v151
	s_waitcnt lgkmcnt(0)
	v_mfma_f32_32x32x16_bf16 v[0:15], v[152:155], v[64:67], v[0:15]
	v_permlane32_swap_b32_e32 v136, v138
	v_permlane32_swap_b32_e32 v137, v139
	v_cvt_pk_bf16_f32 v128, v242, v243
	v_cvt_pk_bf16_f32 v129, v244, v245
	v_cvt_pk_bf16_f32 v130, v156, v157
	v_cvt_pk_bf16_f32 v131, v158, v159
	v_mfma_f32_32x32x16_bf16 v[0:15], v[136:139], v[68:71], v[0:15]
	v_permlane32_swap_b32_e32 v132, v134
	v_permlane32_swap_b32_e32 v133, v135
	ds_read_b64_tr_b16 v[190:191], v205 offset:0x200
	ds_read_b64_tr_b16 v[192:193], v205 offset:0xa00
	ds_read_b64_tr_b16 v[208:209], v205 offset:0x1200
	ds_read_b64_tr_b16 v[210:211], v205 offset:0x1a00
	ds_read_b64_tr_b16 v[238:239], v205 offset:0x2200
	ds_read_b64_tr_b16 v[240:241], v205 offset:0x2a00
	ds_read_b64_tr_b16 v[242:243], v205 offset:0x3200
	ds_read_b64_tr_b16 v[244:245], v205 offset:0x3a00
	v_mfma_f32_32x32x16_bf16 v[0:15], v[132:135], v[72:75], v[0:15]
	v_permlane32_swap_b32_e32 v128, v130
	v_permlane32_swap_b32_e32 v129, v131
	v_permlane32_swap_b32_e32 v203, v204
	v_max_f32_e32 v140, v96, v97
	v_max3_f32 v140, v140, v112, v114
	v_max3_f32 v141, v98, v99, v113
	v_max3_f32 v140, v140, v115, v100
	v_max3_f32 v141, v141, v102, v103
	v_mfma_f32_32x32x16_bf16 v[0:15], v[128:131], v[76:79], v[0:15]
	v_max3_f32 v202, v140, v101, v116
	v_max3_f32 v246, v141, v118, v119
	ds_read_b64_tr_b16 v[156:157], v205 offset:0x400
	ds_read_b64_tr_b16 v[158:159], v205 offset:0xc00
	ds_read_b64_tr_b16 v[148:149], v205 offset:0x1400
	ds_read_b64_tr_b16 v[150:151], v205 offset:0x1c00
	ds_read_b64_tr_b16 v[144:145], v205 offset:0x2400
	ds_read_b64_tr_b16 v[146:147], v205 offset:0x2c00
	ds_read_b64_tr_b16 v[140:141], v205 offset:0x3400
	ds_read_b64_tr_b16 v[142:143], v205 offset:0x3c00
	s_waitcnt lgkmcnt(8)
	v_mfma_f32_32x32x16_bf16 v[48:63], v[152:155], v[190:193], v[48:63]
	v_max3_f32 v190, v202, v117, v104
	v_max3_f32 v191, v246, v106, v107
	v_max3_f32 v190, v190, v105, v120
	v_max3_f32 v191, v191, v122, v123
	v_max3_f32 v190, v190, v121, v108
	v_max3_f32 v191, v191, v110, v111
	v_max3_f32 v190, v190, v109, v124
	v_mfma_f32_32x32x16_bf16 v[48:63], v[136:139], v[208:211], v[48:63]
	v_max3_f32 v191, v191, v126, v127
	v_max3_f32 v190, v190, v125, v191
	v_mov_b32_e32 v191, v190
	s_nop 1
	v_permlane32_swap_b32_e32 v190, v191
	v_mfma_f32_32x32x16_bf16 v[48:63], v[132:135], v[238:241], v[48:63]
	v_max_f32_e32 v238, v190, v191
	v_mfma_f32_32x32x16_bf16 v[48:63], v[128:131], v[242:245], v[48:63]
	s_mov_b32 s2, 0x4138aa3b
	v_cmp_ge_f32_e32 vcc, s2, v238
	s_cmp_eq_u64 vcc, exec
	v_mov_b32_e32 v202, 1.0
	s_cbranch_scc0 .LBB0_860
